# stack + gate/up L0: trailing half's offset barrier moved after the next unit's scheduling math and row-map loads
# speedup vs baseline: 1.0108x; 1.0005x over previous
.LBB0_1535:
	s_add_u32 s16, s8, 0x4fc00000
	s_addc_u32 s17, s9, 0
	s_lshl_b32 s18, s18, 12
	s_lshl_b32 s24, s19, 13
	s_and_b32 s25, s18, 0x3000
	s_mov_b64 s[18:19], 0x80
	s_add_i32 m0, s57, 0x18000
	v_lshl_add_u64 v[6:7], v[6:7], 0, s[18:19]
	s_waitcnt vmcnt(2)
	s_barrier
	global_load_lds_dwordx4 v[6:7], off
	s_add_i32 m0, s57, 0x1a000
	s_add_u32 s20, s8, 0x67c00080
	v_lshl_add_u64 v[4:5], v[4:5], 0, s[18:19]
	s_addc_u32 s21, s9, 0
	s_add_i32 s61, s57, 0x8000
	s_add_i32 s62, s57, 0xa000
	global_load_lds_dwordx4 v[4:5], off
	v_lshl_add_u64 v[4:5], s[20:21], 0, v[142:143]
	s_mov_b32 m0, s61
	s_add_u32 s22, s82, 0x8080
	global_load_lds_dwordx4 v[4:5], off
	v_lshl_add_u64 v[4:5], s[20:21], 0, v[154:155]
	s_mov_b32 m0, s62
	s_addc_u32 s23, s83, 0
	global_load_lds_dwordx4 v[4:5], off
	s_add_i32 m0, s57, 0x1c000
	v_lshl_add_u64 v[4:5], s[22:23], 0, v[138:139]
	global_load_lds_dwordx4 v[4:5], off
	v_lshl_add_u64 v[4:5], s[22:23], 0, v[140:141]
	s_add_i32 m0, s57, 0x1e000
	s_add_i32 s63, s57, 0xc000
	global_load_lds_dwordx4 v[4:5], off
	v_lshl_add_u64 v[4:5], s[20:21], 0, v[152:153]
	s_mov_b32 m0, s63
	s_add_i32 s64, s57, 0xe000
	global_load_lds_dwordx4 v[4:5], off
	v_lshl_add_u64 v[4:5], s[20:21], 0, v[150:151]
	s_mov_b32 m0, s64
	v_readlane_b32 s22, v254, 17
	global_load_lds_dwordx4 v[4:5], off
	v_and_b32_e32 v4, 15, v2
	v_and_b32_e32 v5, 48, v2
	v_lshlrev_b32_e32 v4, 6, v4
	v_lshlrev_b32_e32 v7, 2, v2
	v_readlane_b32 s23, v254, 18
	s_add_u32 s22, s8, s22
	v_or_b32_e32 v6, v4, v5
	v_and_b32_e32 v7, 32, v7
	s_addc_u32 s23, s9, s23
	v_bitop3_b32 v4, v4, v7, v5 bitop3:0x36
	v_bitop3_b32 v5, v6, s24, v7 bitop3:0xde
	s_mov_b32 s24, 0
	v_lshl_add_u64 v[2:3], v[2:3], 4, s[22:23]
	s_mov_b32 s22, 0x72600000
	v_or_b32_e32 v163, s25, v4
	v_add_co_u32_e32 v2, vcc, s22, v2
	s_mov_b32 s25, s24
	s_add_u32 s22, s8, 0x67c00100
	s_mov_b32 s26, s24
	s_mov_b32 s27, s24
	v_mov_b64_e32 v[6:7], s[24:25]
	s_addc_u32 s23, s9, 0
	v_mov_b64_e32 v[8:9], s[26:27]
	s_add_u32 s24, s8, 0x67c00180
	s_addc_u32 s25, s9, 0
	s_cmpk_lt_u32 s7, 0x100
	s_cselect_b64 s[26:27], -1, 0
	s_add_u32 s28, s8, 0x67c00200
	s_addc_u32 s29, s9, 0
	s_add_u32 s30, s8, 0x67c00280
	s_addc_u32 s31, s9, 0
	s_add_u32 s34, s8, 0x67c00300
	s_addc_u32 s35, s9, 0
	v_addc_co_u32_e32 v3, vcc, 0, v3, vcc
	s_add_u32 s36, s8, 0x67c00380
	global_store_dwordx4 v[2:3], v[6:9], off
	global_store_dwordx4 v[2:3], v[6:9], off
	global_store_dwordx4 v[2:3], v[6:9], off
	global_store_dwordx4 v[2:3], v[6:9], off
	s_addc_u32 s37, s9, 0
	s_ashr_i32 s65, s95, 31
	s_ashr_i32 s7, s6, 31
	s_waitcnt vmcnt(12)
	s_add_u32 s38, s2, s95
	s_addc_u32 s39, s96, s65
	s_add_i32 s66, 0, 0x10000
	s_add_i32 s67, 0, 0x14000
	v_add_u32_e32 v164, 0, v5
	v_mov_b64_e32 v[144:145], s[6:7]
	v_add_u32_e32 v165, s66, v163
	v_add_u32_e32 v166, s67, v163
	s_mov_b64 s[40:41], 0x100
	s_mov_b64 s[42:43], 0x180
	s_mov_b64 s[44:45], 0x200
	s_mov_b64 s[46:47], 0x280
	s_mov_b64 s[48:49], 0x300
	s_mov_b64 s[50:51], 0x380
	s_mov_b32 s70, 0xc0c00000
	v_mov_b32_e32 v167, 0x41000000
	s_barrier
	s_mov_b32 s32, 0
	s_branch .LBB0_1538
.LBB0_1536:
	s_mov_b32 s32, 1
	s_add_u32 s38, s38, s95
	s_addc_u32 s39, s39, s65
	s_mov_b64 s[8:9], 0

.LBB0_1542:
	s_cmp_eq_u32 s32, 0
	s_cbranch_scc1 .Lgu0_nobar
	s_andn2_b64 vcc, exec, s[14:15]
	s_cbranch_vccnz .Lgu0_nobar
	s_barrier

.LBB0_1546:
	v_lshlrev_b32_e32 v150, 16, v86
	v_and_b32_e32 v151, 0xffff0000, v86
	v_mul_f32_e32 v158, 0x3d800000, v177
	v_pk_fma_f32 v[130:131], v[158:159], v[130:131], v[150:151] op_sel_hi:[0,1,1]
	v_min_f32_e32 v130, 0x41898193, v130
	v_min_f32_e32 v131, 0x41898193, v131
	v_exp_f32_e64 v178, -v130
	v_exp_f32_e64 v179, -v131
	v_lshlrev_b32_e32 v156, 16, v87
	v_and_b32_e32 v157, 0xffff0000, v87
	v_lshlrev_b32_e32 v152, 16, v82
	v_pk_add_f32 v[178:179], v[178:179], 1.0 op_sel_hi:[1,0]
	v_and_b32_e32 v153, 0xffff0000, v82
	v_rcp_f32_e32 v178, v178
	v_rcp_f32_e32 v179, v179
	v_lshlrev_b32_e32 v154, 16, v83
	v_and_b32_e32 v155, 0xffff0000, v83
	v_pk_fma_f32 v[132:133], v[158:159], v[132:133], v[156:157] op_sel_hi:[0,1,1]
	v_pk_fma_f32 v[134:135], v[158:159], v[134:135], v[152:153] op_sel_hi:[0,1,1]
	v_pk_fma_f32 v[136:137], v[158:159], v[136:137], v[154:155] op_sel_hi:[0,1,1]
	v_med3_f32 v134, v134, s70, v167
	v_med3_f32 v135, v135, s70, v167
	v_pk_mul_f32 v[130:131], v[130:131], v[178:179]
	v_min_f32_e32 v132, 0x41898193, v132
	v_min_f32_e32 v133, 0x41898193, v133
	v_pk_mul_f32 v[130:131], v[130:131], v[134:135]
	v_med3_f32 v134, v136, s70, v167
	v_med3_f32 v135, v137, s70, v167
	v_exp_f32_e64 v136, -v132
	v_exp_f32_e64 v137, -v133
	v_lshlrev_b32_e32 v86, 16, v88
	v_and_b32_e32 v87, 0xffff0000, v88
	v_pk_fma_f32 v[122:123], v[158:159], v[122:123], v[86:87] op_sel_hi:[0,1,1]
	v_pk_add_f32 v[136:137], v[136:137], 1.0 op_sel_hi:[1,0]
	v_min_f32_e32 v122, 0x41898193, v122
	v_rcp_f32_e32 v136, v136
	v_rcp_f32_e32 v137, v137
	v_min_f32_e32 v123, 0x41898193, v123
	v_lshlrev_b32_e32 v88, 16, v89
	v_and_b32_e32 v89, 0xffff0000, v89
	v_pk_mul_f32 v[132:133], v[132:133], v[136:137]
	v_lshlrev_b32_e32 v82, 16, v84
	v_pk_mul_f32 v[132:133], v[132:133], v[134:135]
	v_exp_f32_e64 v134, -v122
	v_exp_f32_e64 v135, -v123
	v_and_b32_e32 v83, 0xffff0000, v84
	v_lshlrev_b32_e32 v84, 16, v85
	v_and_b32_e32 v85, 0xffff0000, v85
	v_pk_add_f32 v[134:135], v[134:135], 1.0 op_sel_hi:[1,0]
	v_pk_fma_f32 v[124:125], v[158:159], v[124:125], v[88:89] op_sel_hi:[0,1,1]
	v_rcp_f32_e32 v134, v134
	v_rcp_f32_e32 v135, v135
	v_pk_fma_f32 v[126:127], v[158:159], v[126:127], v[82:83] op_sel_hi:[0,1,1]
	v_pk_fma_f32 v[128:129], v[158:159], v[128:129], v[84:85] op_sel_hi:[0,1,1]
	v_med3_f32 v126, v126, s70, v167
	v_med3_f32 v127, v127, s70, v167
	v_pk_mul_f32 v[122:123], v[122:123], v[134:135]
	v_min_f32_e32 v124, 0x41898193, v124
	v_min_f32_e32 v125, 0x41898193, v125
	v_pk_mul_f32 v[122:123], v[122:123], v[126:127]
	v_med3_f32 v126, v128, s70, v167
	v_med3_f32 v127, v129, s70, v167
	v_exp_f32_e64 v128, -v124
	v_exp_f32_e64 v129, -v125
	v_mov_b32_e32 v142, v0
	s_and_b64 vcc, exec, s[6:7]
	v_pk_add_f32 v[128:129], v[128:129], 1.0 op_sel_hi:[1,0]
	v_readfirstlane_b32 s69, v142
	v_rcp_f32_e32 v128, v128
	v_rcp_f32_e32 v129, v129
	s_ashr_i32 s8, s69, 6
	s_mul_i32 s9, s8, 0xb00
	s_add_i32 s71, s9, 0
	v_pk_mul_f32 v[124:125], v[124:125], v[128:129]
	v_and_b32_e32 v147, 15, v142
	v_pk_mul_f32 v[124:125], v[124:125], v[126:127]
	v_mov_b32_e32 v126, 0
	v_mov_b32_e32 v127, 0
	v_cvt_pk_fp8_f32 v126, v130, v131
	v_cvt_pk_fp8_f32 v127, v122, v123
	v_lshrrev_b32_e32 v123, 1, v142
	s_add_i32 s71, s71, 0x20000
	v_cvt_pk_fp8_f32 v126, v132, v133 op_sel:[0,0,1]
	v_cvt_pk_fp8_f32 v127, v124, v125 op_sel:[0,0,1]
	v_mul_f32_e32 v124, 0x3d800000, v176
	v_mul_u32_u24_e32 v122, 48, v147
	v_and_b32_e32 v123, 24, v123
	v_pk_fma_f32 v[114:115], v[124:125], v[114:115], v[150:151] op_sel_hi:[0,1,1]
	v_add3_u32 v122, s71, v122, v123
	v_min_f32_e32 v114, 0x41898193, v114
	v_min_f32_e32 v115, 0x41898193, v115
	ds_write_b64 v122, v[126:127]
	v_exp_f32_e64 v126, -v114
	v_exp_f32_e64 v127, -v115
	v_pk_fma_f32 v[116:117], v[124:125], v[116:117], v[156:157] op_sel_hi:[0,1,1]
	v_pk_fma_f32 v[118:119], v[124:125], v[118:119], v[152:153] op_sel_hi:[0,1,1]
	v_pk_fma_f32 v[120:121], v[124:125], v[120:121], v[154:155] op_sel_hi:[0,1,1]
	v_pk_add_f32 v[126:127], v[126:127], 1.0 op_sel_hi:[1,0]
	v_med3_f32 v118, v118, s70, v167
	v_rcp_f32_e32 v126, v126
	v_rcp_f32_e32 v127, v127
	v_med3_f32 v119, v119, s70, v167
	v_min_f32_e32 v116, 0x41898193, v116
	v_min_f32_e32 v117, 0x41898193, v117
	v_pk_mul_f32 v[114:115], v[114:115], v[126:127]
	v_pk_fma_f32 v[106:107], v[124:125], v[106:107], v[86:87] op_sel_hi:[0,1,1]
	v_pk_mul_f32 v[114:115], v[114:115], v[118:119]
	v_med3_f32 v118, v120, s70, v167
	v_med3_f32 v119, v121, s70, v167
	v_exp_f32_e64 v120, -v116
	v_exp_f32_e64 v121, -v117
	v_min_f32_e32 v106, 0x41898193, v106
	v_min_f32_e32 v107, 0x41898193, v107
	v_pk_fma_f32 v[108:109], v[124:125], v[108:109], v[88:89] op_sel_hi:[0,1,1]
	v_pk_add_f32 v[120:121], v[120:121], 1.0 op_sel_hi:[1,0]
	v_pk_fma_f32 v[110:111], v[124:125], v[110:111], v[82:83] op_sel_hi:[0,1,1]
	v_rcp_f32_e32 v120, v120
	v_rcp_f32_e32 v121, v121
	v_pk_fma_f32 v[112:113], v[124:125], v[112:113], v[84:85] op_sel_hi:[0,1,1]
	v_med3_f32 v110, v110, s70, v167
	v_med3_f32 v111, v111, s70, v167
	v_pk_mul_f32 v[116:117], v[116:117], v[120:121]
	v_min_f32_e32 v108, 0x41898193, v108
	v_pk_mul_f32 v[116:117], v[116:117], v[118:119]
	v_exp_f32_e64 v118, -v106
	v_exp_f32_e64 v119, -v107
	v_min_f32_e32 v109, 0x41898193, v109
	s_ashr_i32 s69, s69, 2
	s_andn2_b32 s69, s69, 63
	v_pk_add_f32 v[118:119], v[118:119], 1.0 op_sel_hi:[1,0]
	s_lshl_b32 s8, s8, 5
	v_rcp_f32_e32 v118, v118
	v_rcp_f32_e32 v119, v119
	s_lshl_b32 s9, s80, 7
	s_and_b32 s8, s8, 0x60
	s_or_b32 s8, s8, s9
	v_pk_mul_f32 v[106:107], v[106:107], v[118:119]
	s_ashr_i32 s9, s8, 31
	v_pk_mul_f32 v[106:107], v[106:107], v[110:111]
	v_med3_f32 v110, v112, s70, v167
	v_med3_f32 v111, v113, s70, v167
	v_exp_f32_e64 v112, -v108
	v_exp_f32_e64 v113, -v109
	s_nop 0
	v_pk_add_f32 v[112:113], v[112:113], 1.0 op_sel_hi:[1,0]
	s_nop 0
	v_rcp_f32_e32 v112, v112
	v_rcp_f32_e32 v113, v113
	s_nop 0
	v_pk_mul_f32 v[108:109], v[108:109], v[112:113]
	s_nop 0
	v_pk_mul_f32 v[108:109], v[108:109], v[110:111]
	v_mov_b32_e32 v110, 0
	v_mov_b32_e32 v111, 0
	v_cvt_pk_fp8_f32 v110, v114, v115
	v_cvt_pk_fp8_f32 v111, v106, v107
	v_bfe_u32 v106, v142, 1, 5
	v_mul_u32_u24_e32 v107, 48, v106
	v_cvt_pk_fp8_f32 v110, v116, v117 op_sel:[0,0,1]
	v_cvt_pk_fp8_f32 v111, v108, v109 op_sel:[0,0,1]
	v_lshlrev_b32_e32 v108, 4, v142
	v_and_b32_e32 v142, 16, v108
	v_lshl_or_b32 v106, s78, 8, v106
	ds_write_b64 v122, v[110:111] offset:768
	v_add3_u32 v108, s71, v107, v142
	v_add_u32_e32 v106, s69, v106
	ds_read_b128 v[110:113], v108
	v_ashrrev_i32_e32 v107, 31, v106
	v_lshlrev_b64 v[114:115], 10, v[106:107]
	v_lshl_add_u64 v[114:115], s[16:17], 0, v[114:115]
	v_lshl_add_u64 v[114:115], v[114:115], 0, s[8:9]
	v_lshl_add_u64 v[114:115], v[114:115], 0, v[142:143]
	s_waitcnt lgkmcnt(0)
	global_store_dwordx4 v[114:115], v[110:113], off
	s_nop 1
	v_mul_f32_e32 v110, 0x3d800000, v175
	v_pk_fma_f32 v[98:99], v[110:111], v[98:99], v[150:151] op_sel_hi:[0,1,1]
	v_min_f32_e32 v98, 0x41898193, v98
	v_min_f32_e32 v99, 0x41898193, v99
	v_exp_f32_e64 v112, -v98
	v_exp_f32_e64 v113, -v99
	v_pk_fma_f32 v[100:101], v[110:111], v[100:101], v[156:157] op_sel_hi:[0,1,1]
	v_pk_fma_f32 v[102:103], v[110:111], v[102:103], v[152:153] op_sel_hi:[0,1,1]
	v_pk_fma_f32 v[104:105], v[110:111], v[104:105], v[154:155] op_sel_hi:[0,1,1]
	v_pk_add_f32 v[112:113], v[112:113], 1.0 op_sel_hi:[1,0]
	v_med3_f32 v102, v102, s70, v167
	v_rcp_f32_e32 v112, v112
	v_rcp_f32_e32 v113, v113
	v_med3_f32 v103, v103, s70, v167
	v_min_f32_e32 v100, 0x41898193, v100
	v_min_f32_e32 v101, 0x41898193, v101
	v_pk_mul_f32 v[98:99], v[98:99], v[112:113]
	v_pk_fma_f32 v[90:91], v[110:111], v[90:91], v[86:87] op_sel_hi:[0,1,1]
	v_pk_mul_f32 v[98:99], v[98:99], v[102:103]
	v_med3_f32 v102, v104, s70, v167
	v_med3_f32 v103, v105, s70, v167
	v_exp_f32_e64 v104, -v100
	v_exp_f32_e64 v105, -v101
	v_min_f32_e32 v90, 0x41898193, v90
	v_min_f32_e32 v91, 0x41898193, v91
	v_pk_fma_f32 v[92:93], v[110:111], v[92:93], v[88:89] op_sel_hi:[0,1,1]
	v_pk_add_f32 v[104:105], v[104:105], 1.0 op_sel_hi:[1,0]
	v_pk_fma_f32 v[94:95], v[110:111], v[94:95], v[82:83] op_sel_hi:[0,1,1]
	v_rcp_f32_e32 v104, v104
	v_rcp_f32_e32 v105, v105
	v_pk_fma_f32 v[96:97], v[110:111], v[96:97], v[84:85] op_sel_hi:[0,1,1]
	v_med3_f32 v94, v94, s70, v167
	v_med3_f32 v95, v95, s70, v167
	v_pk_mul_f32 v[100:101], v[100:101], v[104:105]
	v_min_f32_e32 v92, 0x41898193, v92
	v_pk_mul_f32 v[100:101], v[100:101], v[102:103]
	v_exp_f32_e64 v102, -v90
	v_exp_f32_e64 v103, -v91
	v_min_f32_e32 v93, 0x41898193, v93
	v_pk_add_f32 v[102:103], v[102:103], 1.0 op_sel_hi:[1,0]
	s_nop 0
	v_rcp_f32_e32 v102, v102
	v_rcp_f32_e32 v103, v103
	s_nop 0
	v_pk_mul_f32 v[90:91], v[90:91], v[102:103]
	s_nop 0
	v_pk_mul_f32 v[90:91], v[90:91], v[94:95]
	v_med3_f32 v94, v96, s70, v167
	v_med3_f32 v95, v97, s70, v167
	v_exp_f32_e64 v96, -v92
	v_exp_f32_e64 v97, -v93
	s_nop 0
	v_pk_add_f32 v[96:97], v[96:97], 1.0 op_sel_hi:[1,0]
	s_nop 0
	v_rcp_f32_e32 v96, v96
	v_rcp_f32_e32 v97, v97
	s_nop 0
	v_pk_mul_f32 v[92:93], v[92:93], v[96:97]
	s_nop 0
	v_pk_mul_f32 v[92:93], v[92:93], v[94:95]
	v_mov_b32_e32 v95, v143
	v_cvt_pk_fp8_f32 v95, v90, v91
	v_mul_f32_e32 v90, 0x3d800000, v174
	v_pk_fma_f32 v[74:75], v[90:91], v[74:75], v[150:151] op_sel_hi:[0,1,1]
	v_min_f32_e32 v74, 0x41898193, v74
	v_min_f32_e32 v75, 0x41898193, v75
	v_cvt_pk_fp8_f32 v95, v92, v93 op_sel:[0,0,1]
	v_exp_f32_e64 v92, -v74
	v_exp_f32_e64 v93, -v75
	v_pk_fma_f32 v[76:77], v[90:91], v[76:77], v[156:157] op_sel_hi:[0,1,1]
	v_pk_fma_f32 v[78:79], v[90:91], v[78:79], v[152:153] op_sel_hi:[0,1,1]
	v_pk_fma_f32 v[80:81], v[90:91], v[80:81], v[154:155] op_sel_hi:[0,1,1]
	v_pk_add_f32 v[92:93], v[92:93], 1.0 op_sel_hi:[1,0]
	v_med3_f32 v78, v78, s70, v167
	v_rcp_f32_e32 v92, v92
	v_rcp_f32_e32 v93, v93
	v_med3_f32 v79, v79, s70, v167
	v_min_f32_e32 v76, 0x41898193, v76
	v_min_f32_e32 v77, 0x41898193, v77
	v_pk_mul_f32 v[74:75], v[74:75], v[92:93]
	v_pk_fma_f32 v[66:67], v[90:91], v[66:67], v[86:87] op_sel_hi:[0,1,1]
	v_pk_mul_f32 v[74:75], v[74:75], v[78:79]
	v_med3_f32 v78, v80, s70, v167
	v_med3_f32 v79, v81, s70, v167
	v_exp_f32_e64 v80, -v76
	v_exp_f32_e64 v81, -v77
	v_min_f32_e32 v66, 0x41898193, v66
	v_min_f32_e32 v67, 0x41898193, v67
	v_pk_fma_f32 v[68:69], v[90:91], v[68:69], v[88:89] op_sel_hi:[0,1,1]
	v_pk_add_f32 v[80:81], v[80:81], 1.0 op_sel_hi:[1,0]
	v_pk_fma_f32 v[70:71], v[90:91], v[70:71], v[82:83] op_sel_hi:[0,1,1]
	v_rcp_f32_e32 v80, v80
	v_rcp_f32_e32 v81, v81
	v_pk_fma_f32 v[72:73], v[90:91], v[72:73], v[84:85] op_sel_hi:[0,1,1]
	v_med3_f32 v70, v70, s70, v167
	v_med3_f32 v71, v71, s70, v167
	v_pk_mul_f32 v[76:77], v[76:77], v[80:81]
	v_min_f32_e32 v68, 0x41898193, v68
	v_pk_mul_f32 v[76:77], v[76:77], v[78:79]
	v_exp_f32_e64 v78, -v66
	v_exp_f32_e64 v79, -v67
	v_min_f32_e32 v69, 0x41898193, v69
	v_mov_b32_e32 v94, v143
	v_cvt_pk_fp8_f32 v94, v98, v99
	v_pk_add_f32 v[78:79], v[78:79], 1.0 op_sel_hi:[1,0]
	v_cvt_pk_fp8_f32 v94, v100, v101 op_sel:[0,0,1]
	v_rcp_f32_e32 v78, v78
	v_rcp_f32_e32 v79, v79
	ds_write_b64 v122, v[94:95]
	v_pk_mul_f32 v[66:67], v[66:67], v[78:79]
	s_nop 0
	v_pk_mul_f32 v[66:67], v[66:67], v[70:71]
	v_med3_f32 v70, v72, s70, v167
	v_med3_f32 v71, v73, s70, v167
	v_exp_f32_e64 v72, -v68
	v_exp_f32_e64 v73, -v69
	s_nop 0
	v_pk_add_f32 v[72:73], v[72:73], 1.0 op_sel_hi:[1,0]
	s_nop 0
	v_rcp_f32_e32 v72, v72
	v_rcp_f32_e32 v73, v73
	s_nop 0
	v_pk_mul_f32 v[68:69], v[68:69], v[72:73]
	s_nop 0
	v_pk_mul_f32 v[68:69], v[68:69], v[70:71]
	v_mov_b32_e32 v70, v143
	v_mov_b32_e32 v71, v143
	v_cvt_pk_fp8_f32 v70, v74, v75
	v_cvt_pk_fp8_f32 v71, v66, v67
	v_cvt_pk_fp8_f32 v70, v76, v77 op_sel:[0,0,1]
	v_cvt_pk_fp8_f32 v71, v68, v69 op_sel:[0,0,1]
	ds_write_b64 v122, v[70:71] offset:768
	v_or_b32_e32 v70, 32, v106
	ds_read_b128 v[66:69], v108
	v_ashrrev_i32_e32 v71, 31, v70
	v_lshlrev_b64 v[70:71], 10, v[70:71]
	v_lshl_add_u64 v[70:71], s[16:17], 0, v[70:71]
	v_lshl_add_u64 v[70:71], v[70:71], 0, s[8:9]
	v_lshl_add_u64 v[70:71], v[70:71], 0, v[142:143]
	s_waitcnt lgkmcnt(0)
	global_store_dwordx4 v[70:71], v[66:69], off
	s_nop 1
	v_mul_f32_e32 v66, 0x3d800000, v173
	v_pk_fma_f32 v[58:59], v[66:67], v[58:59], v[150:151] op_sel_hi:[0,1,1]
	v_min_f32_e32 v58, 0x41898193, v58
	v_min_f32_e32 v59, 0x41898193, v59
	v_exp_f32_e64 v68, -v58
	v_exp_f32_e64 v69, -v59
	v_pk_fma_f32 v[60:61], v[66:67], v[60:61], v[156:157] op_sel_hi:[0,1,1]
	v_pk_fma_f32 v[62:63], v[66:67], v[62:63], v[152:153] op_sel_hi:[0,1,1]
	v_pk_fma_f32 v[64:65], v[66:67], v[64:65], v[154:155] op_sel_hi:[0,1,1]
	v_pk_add_f32 v[68:69], v[68:69], 1.0 op_sel_hi:[1,0]
	v_med3_f32 v62, v62, s70, v167
	v_rcp_f32_e32 v68, v68
	v_rcp_f32_e32 v69, v69
	v_med3_f32 v63, v63, s70, v167
	v_min_f32_e32 v60, 0x41898193, v60
	v_min_f32_e32 v61, 0x41898193, v61
	v_pk_mul_f32 v[58:59], v[58:59], v[68:69]
	v_pk_fma_f32 v[50:51], v[66:67], v[50:51], v[86:87] op_sel_hi:[0,1,1]
	v_pk_mul_f32 v[58:59], v[58:59], v[62:63]
	v_med3_f32 v62, v64, s70, v167
	v_med3_f32 v63, v65, s70, v167
	v_exp_f32_e64 v64, -v60
	v_exp_f32_e64 v65, -v61
	v_min_f32_e32 v50, 0x41898193, v50
	v_min_f32_e32 v51, 0x41898193, v51
	v_pk_fma_f32 v[52:53], v[66:67], v[52:53], v[88:89] op_sel_hi:[0,1,1]
	v_pk_add_f32 v[64:65], v[64:65], 1.0 op_sel_hi:[1,0]
	v_pk_fma_f32 v[54:55], v[66:67], v[54:55], v[82:83] op_sel_hi:[0,1,1]
	v_rcp_f32_e32 v64, v64
	v_rcp_f32_e32 v65, v65
	v_pk_fma_f32 v[56:57], v[66:67], v[56:57], v[84:85] op_sel_hi:[0,1,1]
	v_med3_f32 v54, v54, s70, v167
	v_med3_f32 v55, v55, s70, v167
	v_pk_mul_f32 v[60:61], v[60:61], v[64:65]
	v_min_f32_e32 v52, 0x41898193, v52
	v_pk_mul_f32 v[60:61], v[60:61], v[62:63]
	v_exp_f32_e64 v62, -v50
	v_exp_f32_e64 v63, -v51
	v_min_f32_e32 v53, 0x41898193, v53
	v_pk_add_f32 v[62:63], v[62:63], 1.0 op_sel_hi:[1,0]
	s_nop 0
	v_rcp_f32_e32 v62, v62
	v_rcp_f32_e32 v63, v63
	s_nop 0
	v_pk_mul_f32 v[50:51], v[50:51], v[62:63]
	s_nop 0
	v_pk_mul_f32 v[50:51], v[50:51], v[54:55]
	v_med3_f32 v54, v56, s70, v167
	v_med3_f32 v55, v57, s70, v167
	v_exp_f32_e64 v56, -v52
	v_exp_f32_e64 v57, -v53
	s_nop 0
	v_pk_add_f32 v[56:57], v[56:57], 1.0 op_sel_hi:[1,0]
	s_nop 0
	v_rcp_f32_e32 v56, v56
	v_rcp_f32_e32 v57, v57
	s_nop 0
	v_pk_mul_f32 v[52:53], v[52:53], v[56:57]
	s_nop 0
	v_pk_mul_f32 v[52:53], v[52:53], v[54:55]
	v_mov_b32_e32 v55, v143
	v_cvt_pk_fp8_f32 v55, v50, v51
	v_mul_f32_e32 v50, 0x3d800000, v172
	v_pk_fma_f32 v[42:43], v[50:51], v[42:43], v[150:151] op_sel_hi:[0,1,1]
	v_min_f32_e32 v42, 0x41898193, v42
	v_min_f32_e32 v43, 0x41898193, v43
	v_cvt_pk_fp8_f32 v55, v52, v53 op_sel:[0,0,1]
	v_exp_f32_e64 v52, -v42
	v_exp_f32_e64 v53, -v43
	v_pk_fma_f32 v[44:45], v[50:51], v[44:45], v[156:157] op_sel_hi:[0,1,1]
	v_pk_fma_f32 v[46:47], v[50:51], v[46:47], v[152:153] op_sel_hi:[0,1,1]
	v_pk_fma_f32 v[48:49], v[50:51], v[48:49], v[154:155] op_sel_hi:[0,1,1]
	v_pk_add_f32 v[52:53], v[52:53], 1.0 op_sel_hi:[1,0]
	v_med3_f32 v46, v46, s70, v167
	v_rcp_f32_e32 v52, v52
	v_rcp_f32_e32 v53, v53
	v_med3_f32 v47, v47, s70, v167
	v_min_f32_e32 v44, 0x41898193, v44
	v_min_f32_e32 v45, 0x41898193, v45
	v_pk_mul_f32 v[42:43], v[42:43], v[52:53]
	v_pk_fma_f32 v[34:35], v[50:51], v[34:35], v[86:87] op_sel_hi:[0,1,1]
	v_pk_mul_f32 v[42:43], v[42:43], v[46:47]
	v_med3_f32 v46, v48, s70, v167
	v_med3_f32 v47, v49, s70, v167
	v_exp_f32_e64 v48, -v44
	v_exp_f32_e64 v49, -v45
	v_min_f32_e32 v34, 0x41898193, v34
	v_min_f32_e32 v35, 0x41898193, v35
	v_pk_fma_f32 v[36:37], v[50:51], v[36:37], v[88:89] op_sel_hi:[0,1,1]
	v_pk_add_f32 v[48:49], v[48:49], 1.0 op_sel_hi:[1,0]
	v_pk_fma_f32 v[38:39], v[50:51], v[38:39], v[82:83] op_sel_hi:[0,1,1]
	v_rcp_f32_e32 v48, v48
	v_rcp_f32_e32 v49, v49
	v_pk_fma_f32 v[40:41], v[50:51], v[40:41], v[84:85] op_sel_hi:[0,1,1]
	v_med3_f32 v38, v38, s70, v167
	v_med3_f32 v39, v39, s70, v167
	v_pk_mul_f32 v[44:45], v[44:45], v[48:49]
	v_min_f32_e32 v36, 0x41898193, v36
	v_pk_mul_f32 v[44:45], v[44:45], v[46:47]
	v_exp_f32_e64 v46, -v34
	v_exp_f32_e64 v47, -v35
	v_min_f32_e32 v37, 0x41898193, v37
	v_mov_b32_e32 v54, v143
	v_cvt_pk_fp8_f32 v54, v58, v59
	v_pk_add_f32 v[46:47], v[46:47], 1.0 op_sel_hi:[1,0]
	v_cvt_pk_fp8_f32 v54, v60, v61 op_sel:[0,0,1]
	v_rcp_f32_e32 v46, v46
	v_rcp_f32_e32 v47, v47
	ds_write_b64 v122, v[54:55]
	v_pk_mul_f32 v[34:35], v[34:35], v[46:47]
	s_nop 0
	v_pk_mul_f32 v[34:35], v[34:35], v[38:39]
	v_med3_f32 v38, v40, s70, v167
	v_med3_f32 v39, v41, s70, v167
	v_exp_f32_e64 v40, -v36
	v_exp_f32_e64 v41, -v37
	s_nop 0
	v_pk_add_f32 v[40:41], v[40:41], 1.0 op_sel_hi:[1,0]
	s_nop 0
	v_rcp_f32_e32 v40, v40
	v_rcp_f32_e32 v41, v41
	s_nop 0
	v_pk_mul_f32 v[36:37], v[36:37], v[40:41]
	s_nop 0
	v_pk_mul_f32 v[36:37], v[36:37], v[38:39]
	v_mov_b32_e32 v38, v143
	v_mov_b32_e32 v39, v143
	v_cvt_pk_fp8_f32 v38, v42, v43
	v_cvt_pk_fp8_f32 v39, v34, v35
	v_cvt_pk_fp8_f32 v38, v44, v45 op_sel:[0,0,1]
	v_cvt_pk_fp8_f32 v39, v36, v37 op_sel:[0,0,1]
	ds_write_b64 v122, v[38:39] offset:768
	v_add_u32_e32 v38, 0x80, v106
	ds_read_b128 v[34:37], v108
	v_ashrrev_i32_e32 v39, 31, v38
	v_lshlrev_b64 v[38:39], 10, v[38:39]
	v_lshl_add_u64 v[38:39], s[16:17], 0, v[38:39]
	v_lshl_add_u64 v[38:39], v[38:39], 0, s[8:9]
	v_lshl_add_u64 v[38:39], v[38:39], 0, v[142:143]
	s_waitcnt lgkmcnt(0)
	global_store_dwordx4 v[38:39], v[34:37], off
	s_nop 1
	v_mul_f32_e32 v34, 0x3d800000, v171
	v_pk_fma_f32 v[26:27], v[34:35], v[26:27], v[150:151] op_sel_hi:[0,1,1]
	v_min_f32_e32 v26, 0x41898193, v26
	v_min_f32_e32 v27, 0x41898193, v27
	v_exp_f32_e64 v36, -v26
	v_exp_f32_e64 v37, -v27
	v_pk_fma_f32 v[28:29], v[34:35], v[28:29], v[156:157] op_sel_hi:[0,1,1]
	v_pk_fma_f32 v[30:31], v[34:35], v[30:31], v[152:153] op_sel_hi:[0,1,1]
	v_pk_fma_f32 v[32:33], v[34:35], v[32:33], v[154:155] op_sel_hi:[0,1,1]
	v_pk_add_f32 v[36:37], v[36:37], 1.0 op_sel_hi:[1,0]
	v_med3_f32 v30, v30, s70, v167
	v_rcp_f32_e32 v36, v36
	v_rcp_f32_e32 v37, v37
	v_med3_f32 v31, v31, s70, v167
	v_min_f32_e32 v28, 0x41898193, v28
	v_min_f32_e32 v29, 0x41898193, v29
	v_pk_mul_f32 v[26:27], v[26:27], v[36:37]
	v_pk_fma_f32 v[18:19], v[34:35], v[18:19], v[86:87] op_sel_hi:[0,1,1]
	v_pk_mul_f32 v[26:27], v[26:27], v[30:31]
	v_med3_f32 v30, v32, s70, v167
	v_med3_f32 v31, v33, s70, v167
	v_exp_f32_e64 v32, -v28
	v_exp_f32_e64 v33, -v29
	v_min_f32_e32 v18, 0x41898193, v18
	v_min_f32_e32 v19, 0x41898193, v19
	v_pk_fma_f32 v[20:21], v[34:35], v[20:21], v[88:89] op_sel_hi:[0,1,1]
	v_pk_add_f32 v[32:33], v[32:33], 1.0 op_sel_hi:[1,0]
	v_pk_fma_f32 v[22:23], v[34:35], v[22:23], v[82:83] op_sel_hi:[0,1,1]
	v_rcp_f32_e32 v32, v32
	v_rcp_f32_e32 v33, v33
	v_pk_fma_f32 v[24:25], v[34:35], v[24:25], v[84:85] op_sel_hi:[0,1,1]
	v_med3_f32 v22, v22, s70, v167
	v_med3_f32 v23, v23, s70, v167
	v_pk_mul_f32 v[28:29], v[28:29], v[32:33]
	v_min_f32_e32 v20, 0x41898193, v20
	v_pk_mul_f32 v[28:29], v[28:29], v[30:31]
	v_exp_f32_e64 v30, -v18
	v_exp_f32_e64 v31, -v19
	v_min_f32_e32 v21, 0x41898193, v21
	v_pk_add_f32 v[30:31], v[30:31], 1.0 op_sel_hi:[1,0]
	s_nop 0
	v_rcp_f32_e32 v30, v30
	v_rcp_f32_e32 v31, v31
	s_nop 0
	v_pk_mul_f32 v[18:19], v[18:19], v[30:31]
	s_nop 0
	v_pk_mul_f32 v[18:19], v[18:19], v[22:23]
	v_med3_f32 v22, v24, s70, v167
	v_med3_f32 v23, v25, s70, v167
	v_exp_f32_e64 v24, -v20
	v_exp_f32_e64 v25, -v21
	s_nop 0
	v_pk_add_f32 v[24:25], v[24:25], 1.0 op_sel_hi:[1,0]
	s_nop 0
	v_rcp_f32_e32 v24, v24
	v_rcp_f32_e32 v25, v25
	s_nop 0
	v_pk_mul_f32 v[20:21], v[20:21], v[24:25]
	s_nop 0
	v_pk_mul_f32 v[20:21], v[20:21], v[22:23]
	v_mov_b32_e32 v23, v143
	v_cvt_pk_fp8_f32 v23, v18, v19
	v_mul_f32_e32 v18, 0x3d800000, v168
	v_pk_fma_f32 v[10:11], v[18:19], v[10:11], v[150:151] op_sel_hi:[0,1,1]
	v_min_f32_e32 v10, 0x41898193, v10
	v_min_f32_e32 v11, 0x41898193, v11
	v_cvt_pk_fp8_f32 v23, v20, v21 op_sel:[0,0,1]
	v_exp_f32_e64 v20, -v10
	v_exp_f32_e64 v21, -v11
	v_pk_fma_f32 v[12:13], v[18:19], v[12:13], v[156:157] op_sel_hi:[0,1,1]
	v_pk_fma_f32 v[14:15], v[18:19], v[14:15], v[152:153] op_sel_hi:[0,1,1]
	v_pk_fma_f32 v[16:17], v[18:19], v[16:17], v[154:155] op_sel_hi:[0,1,1]
	v_pk_add_f32 v[20:21], v[20:21], 1.0 op_sel_hi:[1,0]
	v_med3_f32 v14, v14, s70, v167
	v_rcp_f32_e32 v20, v20
	v_rcp_f32_e32 v21, v21
	v_med3_f32 v15, v15, s70, v167
	v_min_f32_e32 v12, 0x41898193, v12
	v_min_f32_e32 v13, 0x41898193, v13
	v_pk_mul_f32 v[10:11], v[10:11], v[20:21]
	v_pk_fma_f32 v[2:3], v[18:19], v[2:3], v[86:87] op_sel_hi:[0,1,1]
	v_pk_mul_f32 v[10:11], v[10:11], v[14:15]
	v_med3_f32 v14, v16, s70, v167
	v_med3_f32 v15, v17, s70, v167
	v_exp_f32_e64 v16, -v12
	v_exp_f32_e64 v17, -v13
	v_min_f32_e32 v2, 0x41898193, v2
	v_min_f32_e32 v3, 0x41898193, v3
	v_pk_fma_f32 v[4:5], v[18:19], v[4:5], v[88:89] op_sel_hi:[0,1,1]
	v_pk_add_f32 v[16:17], v[16:17], 1.0 op_sel_hi:[1,0]
	v_pk_fma_f32 v[6:7], v[18:19], v[6:7], v[82:83] op_sel_hi:[0,1,1]
	v_rcp_f32_e32 v16, v16
	v_rcp_f32_e32 v17, v17
	v_pk_fma_f32 v[8:9], v[18:19], v[8:9], v[84:85] op_sel_hi:[0,1,1]
	v_med3_f32 v6, v6, s70, v167
	v_med3_f32 v7, v7, s70, v167
	v_pk_mul_f32 v[12:13], v[12:13], v[16:17]
	v_min_f32_e32 v4, 0x41898193, v4
	v_pk_mul_f32 v[12:13], v[12:13], v[14:15]
	v_exp_f32_e64 v14, -v2
	v_exp_f32_e64 v15, -v3
	v_min_f32_e32 v5, 0x41898193, v5
	v_mov_b32_e32 v22, v143
	v_cvt_pk_fp8_f32 v22, v26, v27
	v_pk_add_f32 v[14:15], v[14:15], 1.0 op_sel_hi:[1,0]
	v_cvt_pk_fp8_f32 v22, v28, v29 op_sel:[0,0,1]
	v_rcp_f32_e32 v14, v14
	v_rcp_f32_e32 v15, v15
	ds_write_b64 v122, v[22:23]
	v_pk_mul_f32 v[2:3], v[2:3], v[14:15]
	s_nop 0
	v_pk_mul_f32 v[2:3], v[2:3], v[6:7]
	v_med3_f32 v6, v8, s70, v167
	v_med3_f32 v7, v9, s70, v167
	v_exp_f32_e64 v8, -v4
	v_exp_f32_e64 v9, -v5
	s_nop 0
	v_pk_add_f32 v[8:9], v[8:9], 1.0 op_sel_hi:[1,0]
	s_nop 0
	v_rcp_f32_e32 v8, v8
	v_rcp_f32_e32 v9, v9
	s_nop 0
	v_pk_mul_f32 v[4:5], v[4:5], v[8:9]
	s_nop 0
	v_pk_mul_f32 v[4:5], v[4:5], v[6:7]
	v_mov_b32_e32 v6, v143
	v_mov_b32_e32 v7, v143
	v_cvt_pk_fp8_f32 v6, v10, v11
	v_cvt_pk_fp8_f32 v7, v2, v3
	v_cvt_pk_fp8_f32 v6, v12, v13 op_sel:[0,0,1]
	v_cvt_pk_fp8_f32 v7, v4, v5 op_sel:[0,0,1]
	ds_write_b64 v122, v[6:7] offset:768
	v_add_u32_e32 v6, 0xa0, v106
	ds_read_b128 v[2:5], v108
	v_ashrrev_i32_e32 v7, 31, v6
	v_lshlrev_b64 v[6:7], 10, v[6:7]
	v_lshl_add_u64 v[6:7], s[16:17], 0, v[6:7]
	v_lshl_add_u64 v[6:7], v[6:7], 0, s[8:9]
	v_lshl_add_u64 v[6:7], v[6:7], 0, v[142:143]
	s_mov_b64 s[8:9], -1
	s_waitcnt lgkmcnt(0)
	global_store_dwordx4 v[6:7], v[2:5], off
	s_cbranch_vccnz .LBB0_1537
	s_lshl_b64 s[6:7], s[74:75], 12
	s_add_u32 s9, s33, s6
	s_addc_u32 s69, s54, s7
	s_lshl_b32 s6, s68, 7
	s_ashr_i32 s7, s6, 31
	v_mov_b32_e32 v2, v0
	s_lshl_b64 s[6:7], s[6:7], 1
	s_add_u32 s6, s9, s6
	v_readfirstlane_b32 s8, v2
	s_addc_u32 s7, s69, s7
	s_and_b32 s9, s8, 0xc0
	s_add_u32 s6, s6, s9
	s_addc_u32 s7, s7, 0
	v_and_b32_e32 v3, 48, v2
	global_load_dwordx4 v[86:89], v3, s[6:7]
	global_load_dwordx4 v[82:85], v3, s[6:7] offset:2048
	s_ashr_i32 s7, s8, 2
	s_lshl_b32 s6, s72, 8
	s_andn2_b32 s7, s7, 63
	s_add_i32 s7, s7, s6
	v_and_or_b32 v2, v2, 15, s7
	v_ashrrev_i32_e32 v3, 31, v2
	v_lshl_add_u64 v[4:5], v[2:3], 2, s[12:13]
	v_add_u32_e32 v6, 0x80, v2
	v_add_u32_e32 v8, 0x90, v2
	v_add_u32_e32 v10, 0xa0, v2
	v_add_u32_e32 v2, 0xb0, v2
	v_ashrrev_i32_e32 v7, 31, v6
	v_ashrrev_i32_e32 v9, 31, v8
	v_ashrrev_i32_e32 v11, 31, v10
	v_ashrrev_i32_e32 v3, 31, v2
	v_lshl_add_u64 v[6:7], v[6:7], 2, s[12:13]
	v_lshl_add_u64 v[8:9], v[8:9], 2, s[12:13]
	v_lshl_add_u64 v[10:11], v[10:11], 2, s[12:13]
	v_lshl_add_u64 v[2:3], v[2:3], 2, s[12:13]
	global_load_dword v177, v[4:5], off
	global_load_dword v176, v[4:5], off offset:64
	global_load_dword v175, v[4:5], off offset:128
	global_load_dword v174, v[4:5], off offset:192
	global_load_dword v173, v[6:7], off
	global_load_dword v172, v[8:9], off
	global_load_dword v171, v[10:11], off
	global_load_dword v168, v[2:3], off
	s_andn2_b64 vcc, exec, s[14:15]
	s_cbranch_vccnz .LBB0_1536
	s_nop 0
	s_branch .LBB0_1536
